# P1 projection output stores nt
# speedup vs baseline: 1.0203x; 1.0203x over previous
.LBB0_214:
	s_lshl_b32 s4, s56, 8
	v_mov_b32_e32 v2, v0
	s_add_i32 s4, s4, s72
	s_movk_i32 s40, 0x700
	v_and_or_b32 v144, v2, 15, s4
	v_ashrrev_i32_e32 v145, 31, v144
	v_lshl_add_u64 v[148:149], v[144:145], 2, s[20:21]
	global_load_dword v166, v[148:149], off
	global_load_dword v160, v[148:149], off offset:64
	global_load_dword v158, v[148:149], off offset:128
	global_load_dword v156, v[148:149], off offset:192
	global_load_dword v154, v[148:149], off offset:512
	global_load_dword v152, v[148:149], off offset:576
	global_load_dword v150, v[148:149], off offset:640
	global_load_dword v146, v[148:149], off offset:704
	s_lshl_b32 s4, s77, 8
	s_ashr_i32 s5, s4, 31
	s_lshl_b64 s[12:13], s[4:5], 1
	s_add_u32 s12, s59, s12
	s_addc_u32 s13, s62, s13
	s_add_i32 s56, s4, 0xfffffc00
	s_lshl_b64 s[4:5], s[56:57], 1
	s_add_u32 s4, s63, s4
	s_addc_u32 s5, s68, s5
	s_cmp_lt_i32 s77, 4
	s_cselect_b32 s45, 0x400, s40
	s_cselect_b32 s5, s13, s5
	s_cselect_b32 s4, s12, s4
	s_cmp_lt_i32 s77, 2
	v_bfe_u32 v155, v2, 4, 2
	s_cselect_b64 s[70:71], -1, 0
	s_cmp_eq_u32 s77, 0
	v_lshlrev_b32_e32 v147, 3, v155
	s_cselect_b64 s[64:65], -1, 0
	s_lshl_b32 s12, s77, 2
	v_or_b32_e32 v2, s73, v147
	s_ashr_i32 s13, s12, 31
	v_lshlrev_b32_e32 v2, 1, v2
	s_cmp_eq_u32 s77, 1
	v_lshl_add_u64 v[148:149], s[4:5], 0, v[2:3]
	s_cselect_b64 s[4:5], -1, 0
	s_and_b64 s[60:61], s[36:37], s[4:5]
	v_mad_i64_i32 v[162:163], s[4:5], s45, v144, 0
	v_lshl_add_u64 v[168:169], v[162:163], 1, v[148:149]
	s_cmp_gt_i32 s77, 1
	v_cmp_eq_u32_e64 s[40:41], 0, v155
	s_mov_b32 s80, 0x14000
	s_mov_b32 s79, 0x16000
	s_mov_b32 s78, 0xa000
	s_waitcnt vmcnt(0)
	v_pk_mul_f32 v[130:131], v[130:131], v[166:167] op_sel_hi:[1,0]
	v_pk_mul_f32 v[128:129], v[128:129], v[166:167] op_sel_hi:[1,0]
	v_pk_mul_f32 v[126:127], v[126:127], v[166:167] op_sel_hi:[1,0]
	v_pk_mul_f32 v[124:125], v[124:125], v[166:167] op_sel_hi:[1,0]
	v_cvt_pk_bf16_f32 v162, v128, v129
	v_cvt_pk_bf16_f32 v163, v130, v131
	v_cvt_pk_bf16_f32 v164, v124, v125
	v_cvt_pk_bf16_f32 v165, v126, v127
	v_pk_mul_f32 v[122:123], v[122:123], v[166:167] op_sel_hi:[1,0]
	v_pk_mul_f32 v[120:121], v[120:121], v[166:167] op_sel_hi:[1,0]
	v_pk_mul_f32 v[118:119], v[118:119], v[166:167] op_sel_hi:[1,0]
	v_pk_mul_f32 v[116:117], v[116:117], v[166:167] op_sel_hi:[1,0]
	global_store_dwordx4 v[168:169], v[162:165], off nt
	s_nop 1
	v_cvt_pk_bf16_f32 v162, v120, v121
	v_cvt_pk_bf16_f32 v163, v122, v123
	v_cvt_pk_bf16_f32 v164, v116, v117
	v_cvt_pk_bf16_f32 v165, v118, v119
	global_store_dwordx4 v[168:169], v[162:165], off offset:256 nt
	s_cbranch_scc1 .LBB0_221
	s_nop 0
	v_mov_b32_e32 v163, v124
	v_mov_b32_e32 v124, v129
	v_mov_b32_e32 v129, v126
	v_mov_b32_e32 v126, v131
	v_mov_b32_e32 v162, v128
	v_pk_mul_f32 v[124:125], v[124:125], v[124:125]
	v_mov_b32_e32 v128, v130
	v_pk_mul_f32 v[126:127], v[126:127], v[126:127]
	v_pk_fma_f32 v[124:125], v[162:163], v[162:163], v[124:125]
	v_pk_fma_f32 v[126:127], v[128:129], v[128:129], v[126:127]
	s_andn2_b64 vcc, exec, s[64:65]
	v_pk_add_f32 v[124:125], v[124:125], v[126:127]
	s_nop 0
	v_pk_add_f32 v[124:125], v[124:125], v[124:125] op_sel:[0,1] op_sel_hi:[1,0]
	s_cbranch_vccnz .LBB0_217
	v_mov_b32_e32 v128, v117
	v_mov_b32_e32 v129, v121
	v_mov_b32_e32 v126, v116
	v_mov_b32_e32 v127, v120
	v_pk_mul_f32 v[128:129], v[128:129], v[128:129]
	v_mov_b32_e32 v130, v119
	v_mov_b32_e32 v131, v123
	v_pk_fma_f32 v[126:127], v[126:127], v[126:127], v[128:129]
	v_mov_b32_e32 v128, v118
	v_mov_b32_e32 v129, v122
	v_pk_mul_f32 v[130:131], v[130:131], v[130:131]
	s_nop 0
	v_pk_fma_f32 v[128:129], v[128:129], v[128:129], v[130:131]
	s_nop 0
	v_pk_add_f32 v[126:127], v[126:127], v[128:129]
	s_nop 0
	v_add_f32_e32 v2, v127, v124
	v_add_f32_e32 v124, v126, v2

.LBB0_219:
	s_or_b64 exec, exec, s[4:5]
	s_andn2_b64 vcc, exec, s[60:61]
	s_cbranch_vccnz .LBB0_221
	s_waitcnt lgkmcnt(0)
	v_lshlrev_b64 v[124:125], 7, v[144:145]
	v_lshl_add_u64 v[124:125], s[18:19], 0, v[124:125]
	v_lshlrev_b32_e32 v2, 2, v147
	v_lshl_add_u64 v[124:125], v[124:125], 0, v[2:3]
	global_store_dwordx4 v[124:125], v[120:123], off nt
	global_store_dwordx4 v[124:125], v[116:119], off offset:16 nt
.LBB0_221:
	s_nop 1
	v_or_b32_e32 v116, 16, v144
	v_mad_i64_i32 v[118:119], s[4:5], s45, v116, 0
	v_pk_mul_f32 v[114:115], v[114:115], v[160:161] op_sel_hi:[1,0]
	v_pk_mul_f32 v[112:113], v[112:113], v[160:161] op_sel_hi:[1,0]
	v_pk_mul_f32 v[110:111], v[110:111], v[160:161] op_sel_hi:[1,0]
	v_pk_mul_f32 v[108:109], v[108:109], v[160:161] op_sel_hi:[1,0]
	v_lshl_add_u64 v[122:123], v[118:119], 1, v[148:149]
	v_cvt_pk_bf16_f32 v118, v112, v113
	v_cvt_pk_bf16_f32 v119, v114, v115
	v_cvt_pk_bf16_f32 v120, v108, v109
	v_cvt_pk_bf16_f32 v121, v110, v111
	v_pk_mul_f32 v[106:107], v[106:107], v[160:161] op_sel_hi:[1,0]
	v_pk_mul_f32 v[104:105], v[104:105], v[160:161] op_sel_hi:[1,0]
	v_pk_mul_f32 v[102:103], v[102:103], v[160:161] op_sel_hi:[1,0]
	v_pk_mul_f32 v[100:101], v[100:101], v[160:161] op_sel_hi:[1,0]
	v_cndmask_b32_e64 v2, 0, 1, s[70:71]
	global_store_dwordx4 v[122:123], v[118:121], off nt
	v_cmp_ne_u32_e64 s[42:43], 1, v2
	s_andn2_b64 vcc, exec, s[70:71]
	v_cvt_pk_bf16_f32 v118, v104, v105
	v_cvt_pk_bf16_f32 v119, v106, v107
	v_cvt_pk_bf16_f32 v120, v100, v101
	v_cvt_pk_bf16_f32 v121, v102, v103
	v_readlane_b32 s84, v255, 35
	s_mov_b32 s81, 0x8000
	s_mov_b32 s82, 0x10000
	s_mov_b32 s83, 0x12000
	global_store_dwordx4 v[122:123], v[118:121], off offset:256 nt
	s_cbranch_vccnz .LBB0_228
	s_nop 0
	v_mov_b32_e32 v119, v108
	v_mov_b32_e32 v108, v113
	v_mov_b32_e32 v113, v110
	v_mov_b32_e32 v110, v115
	v_mov_b32_e32 v118, v112
	v_pk_mul_f32 v[108:109], v[108:109], v[108:109]
	v_mov_b32_e32 v112, v114
	v_pk_mul_f32 v[110:111], v[110:111], v[110:111]
	v_pk_fma_f32 v[108:109], v[118:119], v[118:119], v[108:109]
	v_pk_fma_f32 v[110:111], v[112:113], v[112:113], v[110:111]
	s_andn2_b64 vcc, exec, s[64:65]
	v_pk_add_f32 v[108:109], v[108:109], v[110:111]
	s_nop 0
	v_pk_add_f32 v[108:109], v[108:109], v[108:109] op_sel:[0,1] op_sel_hi:[1,0]
	s_cbranch_vccnz .LBB0_224
	v_mov_b32_e32 v112, v101
	v_mov_b32_e32 v113, v105
	v_mov_b32_e32 v110, v100
	v_mov_b32_e32 v111, v104
	v_pk_mul_f32 v[112:113], v[112:113], v[112:113]
	v_mov_b32_e32 v114, v103
	v_mov_b32_e32 v115, v107
	v_pk_fma_f32 v[110:111], v[110:111], v[110:111], v[112:113]
	v_mov_b32_e32 v112, v102
	v_mov_b32_e32 v113, v106
	v_pk_mul_f32 v[114:115], v[114:115], v[114:115]
	s_nop 0
	v_pk_fma_f32 v[112:113], v[112:113], v[112:113], v[114:115]
	s_nop 0
	v_pk_add_f32 v[110:111], v[110:111], v[112:113]
	s_nop 0
	v_add_f32_e32 v2, v111, v108
	v_add_f32_e32 v108, v110, v2

.LBB0_226:
	s_or_b64 exec, exec, s[4:5]
	s_andn2_b64 vcc, exec, s[60:61]
	s_cbranch_vccnz .LBB0_228
	s_waitcnt lgkmcnt(0)
	v_lshlrev_b64 v[108:109], 7, v[116:117]
	v_lshl_add_u64 v[108:109], s[18:19], 0, v[108:109]
	v_lshlrev_b32_e32 v2, 2, v147
	v_lshl_add_u64 v[108:109], v[108:109], 0, v[2:3]
	global_store_dwordx4 v[108:109], v[104:107], off nt
	global_store_dwordx4 v[108:109], v[100:103], off offset:16 nt
.LBB0_228:
	s_nop 1
	v_or_b32_e32 v100, 32, v144
	v_mad_i64_i32 v[102:103], s[4:5], s45, v100, 0
	v_pk_mul_f32 v[98:99], v[98:99], v[158:159] op_sel_hi:[1,0]
	v_pk_mul_f32 v[96:97], v[96:97], v[158:159] op_sel_hi:[1,0]
	v_pk_mul_f32 v[94:95], v[94:95], v[158:159] op_sel_hi:[1,0]
	v_pk_mul_f32 v[92:93], v[92:93], v[158:159] op_sel_hi:[1,0]
	v_lshl_add_u64 v[106:107], v[102:103], 1, v[148:149]
	v_cvt_pk_bf16_f32 v102, v96, v97
	v_cvt_pk_bf16_f32 v103, v98, v99
	v_cvt_pk_bf16_f32 v104, v92, v93
	v_cvt_pk_bf16_f32 v105, v94, v95
	v_pk_mul_f32 v[90:91], v[90:91], v[158:159] op_sel_hi:[1,0]
	v_pk_mul_f32 v[88:89], v[88:89], v[158:159] op_sel_hi:[1,0]
	v_pk_mul_f32 v[86:87], v[86:87], v[158:159] op_sel_hi:[1,0]
	v_pk_mul_f32 v[84:85], v[84:85], v[158:159] op_sel_hi:[1,0]
	global_store_dwordx4 v[106:107], v[102:105], off nt
	s_and_b64 vcc, exec, s[42:43]
	s_nop 0
	v_cvt_pk_bf16_f32 v102, v88, v89
	v_cvt_pk_bf16_f32 v103, v90, v91
	v_cvt_pk_bf16_f32 v104, v84, v85
	v_cvt_pk_bf16_f32 v105, v86, v87
	global_store_dwordx4 v[106:107], v[102:105], off offset:256 nt
	s_cbranch_vccnz .LBB0_235
	s_nop 0
	v_mov_b32_e32 v103, v92
	v_mov_b32_e32 v92, v97
	v_mov_b32_e32 v97, v94
	v_mov_b32_e32 v94, v99
	v_mov_b32_e32 v102, v96
	v_pk_mul_f32 v[92:93], v[92:93], v[92:93]
	v_mov_b32_e32 v96, v98
	v_pk_mul_f32 v[94:95], v[94:95], v[94:95]
	v_pk_fma_f32 v[92:93], v[102:103], v[102:103], v[92:93]
	v_pk_fma_f32 v[94:95], v[96:97], v[96:97], v[94:95]
	s_andn2_b64 vcc, exec, s[64:65]
	v_pk_add_f32 v[92:93], v[92:93], v[94:95]
	s_nop 0
	v_pk_add_f32 v[92:93], v[92:93], v[92:93] op_sel:[0,1] op_sel_hi:[1,0]
	s_cbranch_vccnz .LBB0_231
	v_mov_b32_e32 v96, v85
	v_mov_b32_e32 v97, v89
	v_mov_b32_e32 v94, v84
	v_mov_b32_e32 v95, v88
	v_pk_mul_f32 v[96:97], v[96:97], v[96:97]
	v_mov_b32_e32 v98, v87
	v_mov_b32_e32 v99, v91
	v_pk_fma_f32 v[94:95], v[94:95], v[94:95], v[96:97]
	v_mov_b32_e32 v96, v86
	v_mov_b32_e32 v97, v90
	v_pk_mul_f32 v[98:99], v[98:99], v[98:99]
	s_nop 0
	v_pk_fma_f32 v[96:97], v[96:97], v[96:97], v[98:99]
	s_nop 0
	v_pk_add_f32 v[94:95], v[94:95], v[96:97]
	s_nop 0
	v_add_f32_e32 v2, v95, v92
	v_add_f32_e32 v92, v94, v2

.LBB0_233:
	s_or_b64 exec, exec, s[4:5]
	s_andn2_b64 vcc, exec, s[60:61]
	s_cbranch_vccnz .LBB0_235
	s_waitcnt lgkmcnt(0)
	v_lshlrev_b64 v[92:93], 7, v[100:101]
	v_lshl_add_u64 v[92:93], s[18:19], 0, v[92:93]
	v_lshlrev_b32_e32 v2, 2, v147
	v_lshl_add_u64 v[92:93], v[92:93], 0, v[2:3]
	global_store_dwordx4 v[92:93], v[88:91], off nt
	global_store_dwordx4 v[92:93], v[84:87], off offset:16 nt
.LBB0_235:
	s_nop 1
	v_or_b32_e32 v84, 48, v144
	v_mad_i64_i32 v[86:87], s[4:5], s45, v84, 0
	v_pk_mul_f32 v[82:83], v[82:83], v[156:157] op_sel_hi:[1,0]
	v_pk_mul_f32 v[80:81], v[80:81], v[156:157] op_sel_hi:[1,0]
	v_pk_mul_f32 v[78:79], v[78:79], v[156:157] op_sel_hi:[1,0]
	v_pk_mul_f32 v[76:77], v[76:77], v[156:157] op_sel_hi:[1,0]
	v_lshl_add_u64 v[90:91], v[86:87], 1, v[148:149]
	v_cvt_pk_bf16_f32 v86, v80, v81
	v_cvt_pk_bf16_f32 v87, v82, v83
	v_cvt_pk_bf16_f32 v88, v76, v77
	v_cvt_pk_bf16_f32 v89, v78, v79
	v_pk_mul_f32 v[74:75], v[74:75], v[156:157] op_sel_hi:[1,0]
	v_pk_mul_f32 v[72:73], v[72:73], v[156:157] op_sel_hi:[1,0]
	v_pk_mul_f32 v[70:71], v[70:71], v[156:157] op_sel_hi:[1,0]
	v_pk_mul_f32 v[68:69], v[68:69], v[156:157] op_sel_hi:[1,0]
	global_store_dwordx4 v[90:91], v[86:89], off nt
	s_and_b64 vcc, exec, s[42:43]
	s_nop 0
	v_cvt_pk_bf16_f32 v86, v72, v73
	v_cvt_pk_bf16_f32 v87, v74, v75
	v_cvt_pk_bf16_f32 v88, v68, v69
	v_cvt_pk_bf16_f32 v89, v70, v71
	global_store_dwordx4 v[90:91], v[86:89], off offset:256 nt
	s_cbranch_vccnz .LBB0_242
	s_nop 0
	v_mov_b32_e32 v87, v76
	v_mov_b32_e32 v76, v81
	v_mov_b32_e32 v81, v78
	v_mov_b32_e32 v78, v83
	v_mov_b32_e32 v86, v80
	v_pk_mul_f32 v[76:77], v[76:77], v[76:77]
	v_mov_b32_e32 v80, v82
	v_pk_mul_f32 v[78:79], v[78:79], v[78:79]
	v_pk_fma_f32 v[76:77], v[86:87], v[86:87], v[76:77]
	v_pk_fma_f32 v[78:79], v[80:81], v[80:81], v[78:79]
	s_andn2_b64 vcc, exec, s[64:65]
	v_pk_add_f32 v[76:77], v[76:77], v[78:79]
	s_nop 0
	v_pk_add_f32 v[76:77], v[76:77], v[76:77] op_sel:[0,1] op_sel_hi:[1,0]
	s_cbranch_vccnz .LBB0_238
	v_mov_b32_e32 v80, v69
	v_mov_b32_e32 v81, v73
	v_mov_b32_e32 v78, v68
	v_mov_b32_e32 v79, v72
	v_pk_mul_f32 v[80:81], v[80:81], v[80:81]
	v_mov_b32_e32 v82, v71
	v_mov_b32_e32 v83, v75
	v_pk_fma_f32 v[78:79], v[78:79], v[78:79], v[80:81]
	v_mov_b32_e32 v80, v70
	v_mov_b32_e32 v81, v74
	v_pk_mul_f32 v[82:83], v[82:83], v[82:83]
	s_nop 0
	v_pk_fma_f32 v[80:81], v[80:81], v[80:81], v[82:83]
	s_nop 0
	v_pk_add_f32 v[78:79], v[78:79], v[80:81]
	s_nop 0
	v_add_f32_e32 v2, v79, v76
	v_add_f32_e32 v76, v78, v2

.LBB0_240:
	s_or_b64 exec, exec, s[4:5]
	s_andn2_b64 vcc, exec, s[60:61]
	s_cbranch_vccnz .LBB0_242
	s_waitcnt lgkmcnt(0)
	v_lshlrev_b64 v[76:77], 7, v[84:85]
	v_lshl_add_u64 v[76:77], s[18:19], 0, v[76:77]
	v_lshlrev_b32_e32 v2, 2, v147
	v_lshl_add_u64 v[76:77], v[76:77], 0, v[2:3]
	global_store_dwordx4 v[76:77], v[72:75], off nt
	global_store_dwordx4 v[76:77], v[68:71], off offset:16 nt
.LBB0_242:
	s_nop 1
	v_add_u32_e32 v68, 0x80, v144
	v_mad_i64_i32 v[70:71], s[4:5], s45, v68, 0
	v_pk_mul_f32 v[66:67], v[66:67], v[154:155] op_sel_hi:[1,0]
	v_pk_mul_f32 v[64:65], v[64:65], v[154:155] op_sel_hi:[1,0]
	v_pk_mul_f32 v[62:63], v[62:63], v[154:155] op_sel_hi:[1,0]
	v_pk_mul_f32 v[60:61], v[60:61], v[154:155] op_sel_hi:[1,0]
	v_lshl_add_u64 v[74:75], v[70:71], 1, v[148:149]
	v_cvt_pk_bf16_f32 v70, v64, v65
	v_cvt_pk_bf16_f32 v71, v66, v67
	v_cvt_pk_bf16_f32 v72, v60, v61
	v_cvt_pk_bf16_f32 v73, v62, v63
	v_pk_mul_f32 v[58:59], v[58:59], v[154:155] op_sel_hi:[1,0]
	v_pk_mul_f32 v[56:57], v[56:57], v[154:155] op_sel_hi:[1,0]
	v_pk_mul_f32 v[54:55], v[54:55], v[154:155] op_sel_hi:[1,0]
	v_pk_mul_f32 v[52:53], v[52:53], v[154:155] op_sel_hi:[1,0]
	global_store_dwordx4 v[74:75], v[70:73], off nt
	s_and_b64 vcc, exec, s[42:43]
	s_nop 0
	v_cvt_pk_bf16_f32 v70, v56, v57
	v_cvt_pk_bf16_f32 v71, v58, v59
	v_cvt_pk_bf16_f32 v72, v52, v53
	v_cvt_pk_bf16_f32 v73, v54, v55
	global_store_dwordx4 v[74:75], v[70:73], off offset:256 nt
	s_cbranch_vccnz .LBB0_249
	s_nop 0
	v_mov_b32_e32 v71, v60
	v_mov_b32_e32 v60, v65
	v_mov_b32_e32 v65, v62
	v_mov_b32_e32 v62, v67
	v_mov_b32_e32 v70, v64
	v_pk_mul_f32 v[60:61], v[60:61], v[60:61]
	v_mov_b32_e32 v64, v66
	v_pk_mul_f32 v[62:63], v[62:63], v[62:63]
	v_pk_fma_f32 v[60:61], v[70:71], v[70:71], v[60:61]
	v_pk_fma_f32 v[62:63], v[64:65], v[64:65], v[62:63]
	s_andn2_b64 vcc, exec, s[64:65]
	v_pk_add_f32 v[60:61], v[60:61], v[62:63]
	s_nop 0
	v_pk_add_f32 v[60:61], v[60:61], v[60:61] op_sel:[0,1] op_sel_hi:[1,0]
	s_cbranch_vccnz .LBB0_245
	v_mov_b32_e32 v64, v53
	v_mov_b32_e32 v65, v57
	v_mov_b32_e32 v62, v52
	v_mov_b32_e32 v63, v56
	v_pk_mul_f32 v[64:65], v[64:65], v[64:65]
	v_mov_b32_e32 v66, v55
	v_mov_b32_e32 v67, v59
	v_pk_fma_f32 v[62:63], v[62:63], v[62:63], v[64:65]
	v_mov_b32_e32 v64, v54
	v_mov_b32_e32 v65, v58
	v_pk_mul_f32 v[66:67], v[66:67], v[66:67]
	s_nop 0
	v_pk_fma_f32 v[64:65], v[64:65], v[64:65], v[66:67]
	s_nop 0
	v_pk_add_f32 v[62:63], v[62:63], v[64:65]
	s_nop 0
	v_add_f32_e32 v2, v63, v60
	v_add_f32_e32 v60, v62, v2

.LBB0_247:
	s_or_b64 exec, exec, s[4:5]
	s_andn2_b64 vcc, exec, s[60:61]
	s_cbranch_vccnz .LBB0_249
	s_waitcnt lgkmcnt(0)
	v_lshlrev_b64 v[60:61], 7, v[68:69]
	v_lshl_add_u64 v[60:61], s[18:19], 0, v[60:61]
	v_lshlrev_b32_e32 v2, 2, v147
	v_lshl_add_u64 v[60:61], v[60:61], 0, v[2:3]
	global_store_dwordx4 v[60:61], v[56:59], off nt
	global_store_dwordx4 v[60:61], v[52:55], off offset:16 nt
.LBB0_249:
	s_nop 1
	v_add_u32_e32 v52, 0x90, v144
	v_mad_i64_i32 v[54:55], s[4:5], s45, v52, 0
	v_pk_mul_f32 v[50:51], v[50:51], v[152:153] op_sel_hi:[1,0]
	v_pk_mul_f32 v[48:49], v[48:49], v[152:153] op_sel_hi:[1,0]
	v_pk_mul_f32 v[46:47], v[46:47], v[152:153] op_sel_hi:[1,0]
	v_pk_mul_f32 v[44:45], v[44:45], v[152:153] op_sel_hi:[1,0]
	v_lshl_add_u64 v[58:59], v[54:55], 1, v[148:149]
	v_cvt_pk_bf16_f32 v54, v48, v49
	v_cvt_pk_bf16_f32 v55, v50, v51
	v_cvt_pk_bf16_f32 v56, v44, v45
	v_cvt_pk_bf16_f32 v57, v46, v47
	v_pk_mul_f32 v[42:43], v[42:43], v[152:153] op_sel_hi:[1,0]
	v_pk_mul_f32 v[40:41], v[40:41], v[152:153] op_sel_hi:[1,0]
	v_pk_mul_f32 v[38:39], v[38:39], v[152:153] op_sel_hi:[1,0]
	v_pk_mul_f32 v[36:37], v[36:37], v[152:153] op_sel_hi:[1,0]
	global_store_dwordx4 v[58:59], v[54:57], off nt
	s_and_b64 vcc, exec, s[42:43]
	s_nop 0
	v_cvt_pk_bf16_f32 v54, v40, v41
	v_cvt_pk_bf16_f32 v55, v42, v43
	v_cvt_pk_bf16_f32 v56, v36, v37
	v_cvt_pk_bf16_f32 v57, v38, v39
	global_store_dwordx4 v[58:59], v[54:57], off offset:256 nt
	s_cbranch_vccnz .LBB0_256
	s_nop 0
	v_mov_b32_e32 v55, v44
	v_mov_b32_e32 v44, v49
	v_mov_b32_e32 v49, v46
	v_mov_b32_e32 v46, v51
	v_mov_b32_e32 v54, v48
	v_pk_mul_f32 v[44:45], v[44:45], v[44:45]
	v_mov_b32_e32 v48, v50
	v_pk_mul_f32 v[46:47], v[46:47], v[46:47]
	v_pk_fma_f32 v[44:45], v[54:55], v[54:55], v[44:45]
	v_pk_fma_f32 v[46:47], v[48:49], v[48:49], v[46:47]
	s_andn2_b64 vcc, exec, s[64:65]
	v_pk_add_f32 v[44:45], v[44:45], v[46:47]
	s_nop 0
	v_pk_add_f32 v[44:45], v[44:45], v[44:45] op_sel:[0,1] op_sel_hi:[1,0]
	s_cbranch_vccnz .LBB0_252
	v_mov_b32_e32 v48, v37
	v_mov_b32_e32 v49, v41
	v_mov_b32_e32 v46, v36
	v_mov_b32_e32 v47, v40
	v_pk_mul_f32 v[48:49], v[48:49], v[48:49]
	v_mov_b32_e32 v50, v39
	v_mov_b32_e32 v51, v43
	v_pk_fma_f32 v[46:47], v[46:47], v[46:47], v[48:49]
	v_mov_b32_e32 v48, v38
	v_mov_b32_e32 v49, v42
	v_pk_mul_f32 v[50:51], v[50:51], v[50:51]
	s_nop 0
	v_pk_fma_f32 v[48:49], v[48:49], v[48:49], v[50:51]
	s_nop 0
	v_pk_add_f32 v[46:47], v[46:47], v[48:49]
	s_nop 0
	v_add_f32_e32 v2, v47, v44
	v_add_f32_e32 v44, v46, v2

.LBB0_254:
	s_or_b64 exec, exec, s[4:5]
	s_andn2_b64 vcc, exec, s[60:61]
	s_cbranch_vccnz .LBB0_256
	s_waitcnt lgkmcnt(0)
	v_lshlrev_b64 v[44:45], 7, v[52:53]
	v_lshl_add_u64 v[44:45], s[18:19], 0, v[44:45]
	v_lshlrev_b32_e32 v2, 2, v147
	v_lshl_add_u64 v[44:45], v[44:45], 0, v[2:3]
	global_store_dwordx4 v[44:45], v[40:43], off nt
	global_store_dwordx4 v[44:45], v[36:39], off offset:16 nt
.LBB0_256:
	s_nop 1
	v_add_u32_e32 v36, 0xa0, v144
	v_mad_i64_i32 v[38:39], s[4:5], s45, v36, 0
	v_pk_mul_f32 v[34:35], v[34:35], v[150:151] op_sel_hi:[1,0]
	v_pk_mul_f32 v[32:33], v[32:33], v[150:151] op_sel_hi:[1,0]
	v_pk_mul_f32 v[30:31], v[30:31], v[150:151] op_sel_hi:[1,0]
	v_pk_mul_f32 v[28:29], v[28:29], v[150:151] op_sel_hi:[1,0]
	v_lshl_add_u64 v[42:43], v[38:39], 1, v[148:149]
	v_cvt_pk_bf16_f32 v38, v32, v33
	v_cvt_pk_bf16_f32 v39, v34, v35
	v_cvt_pk_bf16_f32 v40, v28, v29
	v_cvt_pk_bf16_f32 v41, v30, v31
	v_pk_mul_f32 v[26:27], v[26:27], v[150:151] op_sel_hi:[1,0]
	v_pk_mul_f32 v[24:25], v[24:25], v[150:151] op_sel_hi:[1,0]
	v_pk_mul_f32 v[22:23], v[22:23], v[150:151] op_sel_hi:[1,0]
	v_pk_mul_f32 v[20:21], v[20:21], v[150:151] op_sel_hi:[1,0]
	global_store_dwordx4 v[42:43], v[38:41], off nt
	s_and_b64 vcc, exec, s[42:43]
	s_nop 0
	v_cvt_pk_bf16_f32 v38, v24, v25
	v_cvt_pk_bf16_f32 v39, v26, v27
	v_cvt_pk_bf16_f32 v40, v20, v21
	v_cvt_pk_bf16_f32 v41, v22, v23
	global_store_dwordx4 v[42:43], v[38:41], off offset:256 nt
	s_cbranch_vccnz .LBB0_263
	s_nop 0
	v_mov_b32_e32 v39, v28
	v_mov_b32_e32 v28, v33
	v_mov_b32_e32 v33, v30
	v_mov_b32_e32 v30, v35
	v_mov_b32_e32 v38, v32
	v_pk_mul_f32 v[28:29], v[28:29], v[28:29]
	v_mov_b32_e32 v32, v34
	v_pk_mul_f32 v[30:31], v[30:31], v[30:31]
	v_pk_fma_f32 v[28:29], v[38:39], v[38:39], v[28:29]
	v_pk_fma_f32 v[30:31], v[32:33], v[32:33], v[30:31]
	s_andn2_b64 vcc, exec, s[64:65]
	v_pk_add_f32 v[28:29], v[28:29], v[30:31]
	s_nop 0
	v_pk_add_f32 v[28:29], v[28:29], v[28:29] op_sel:[0,1] op_sel_hi:[1,0]
	s_cbranch_vccnz .LBB0_259
	v_mov_b32_e32 v32, v21
	v_mov_b32_e32 v33, v25
	v_mov_b32_e32 v30, v20
	v_mov_b32_e32 v31, v24
	v_pk_mul_f32 v[32:33], v[32:33], v[32:33]
	v_mov_b32_e32 v34, v23
	v_mov_b32_e32 v35, v27
	v_pk_fma_f32 v[30:31], v[30:31], v[30:31], v[32:33]
	v_mov_b32_e32 v32, v22
	v_mov_b32_e32 v33, v26
	v_pk_mul_f32 v[34:35], v[34:35], v[34:35]
	s_nop 0
	v_pk_fma_f32 v[32:33], v[32:33], v[32:33], v[34:35]
	s_nop 0
	v_pk_add_f32 v[30:31], v[30:31], v[32:33]
	s_nop 0
	v_add_f32_e32 v2, v31, v28
	v_add_f32_e32 v28, v30, v2

.LBB0_261:
	s_or_b64 exec, exec, s[4:5]
	s_andn2_b64 vcc, exec, s[60:61]
	s_cbranch_vccnz .LBB0_263
	s_waitcnt lgkmcnt(0)
	v_lshlrev_b64 v[28:29], 7, v[36:37]
	v_lshl_add_u64 v[28:29], s[18:19], 0, v[28:29]
	v_lshlrev_b32_e32 v2, 2, v147
	v_lshl_add_u64 v[28:29], v[28:29], 0, v[2:3]
	global_store_dwordx4 v[28:29], v[24:27], off nt
	global_store_dwordx4 v[28:29], v[20:23], off offset:16 nt
.LBB0_263:
	s_nop 1
	v_add_u32_e32 v20, 0xb0, v144
	v_mad_i64_i32 v[22:23], s[4:5], s45, v20, 0
	v_pk_mul_f32 v[18:19], v[18:19], v[146:147] op_sel_hi:[1,0]
	v_pk_mul_f32 v[16:17], v[16:17], v[146:147] op_sel_hi:[1,0]
	v_pk_mul_f32 v[14:15], v[14:15], v[146:147] op_sel_hi:[1,0]
	v_pk_mul_f32 v[12:13], v[12:13], v[146:147] op_sel_hi:[1,0]
	v_lshl_add_u64 v[26:27], v[22:23], 1, v[148:149]
	v_cvt_pk_bf16_f32 v22, v16, v17
	v_cvt_pk_bf16_f32 v23, v18, v19
	v_cvt_pk_bf16_f32 v24, v12, v13
	v_cvt_pk_bf16_f32 v25, v14, v15
	v_pk_mul_f32 v[10:11], v[10:11], v[146:147] op_sel_hi:[1,0]
	v_pk_mul_f32 v[8:9], v[8:9], v[146:147] op_sel_hi:[1,0]
	v_pk_mul_f32 v[6:7], v[6:7], v[146:147] op_sel_hi:[1,0]
	v_pk_mul_f32 v[4:5], v[4:5], v[146:147] op_sel_hi:[1,0]
	global_store_dwordx4 v[26:27], v[22:25], off nt
	s_and_b64 vcc, exec, s[42:43]
	s_nop 0
	v_cvt_pk_bf16_f32 v22, v8, v9
	v_cvt_pk_bf16_f32 v23, v10, v11
	v_cvt_pk_bf16_f32 v24, v4, v5
	v_cvt_pk_bf16_f32 v25, v6, v7
	global_store_dwordx4 v[26:27], v[22:25], off offset:256 nt
	s_cbranch_vccnz .LBB0_270
	s_nop 0
	v_mov_b32_e32 v23, v12
	v_mov_b32_e32 v12, v17
	v_mov_b32_e32 v17, v14
	v_mov_b32_e32 v14, v19
	v_mov_b32_e32 v22, v16
	v_pk_mul_f32 v[12:13], v[12:13], v[12:13]
	v_mov_b32_e32 v16, v18
	v_pk_mul_f32 v[14:15], v[14:15], v[14:15]
	v_pk_fma_f32 v[12:13], v[22:23], v[22:23], v[12:13]
	v_pk_fma_f32 v[14:15], v[16:17], v[16:17], v[14:15]
	s_andn2_b64 vcc, exec, s[64:65]
	v_pk_add_f32 v[12:13], v[12:13], v[14:15]
	s_nop 0
	v_pk_add_f32 v[12:13], v[12:13], v[12:13] op_sel:[0,1] op_sel_hi:[1,0]
	s_cbranch_vccnz .LBB0_266
	v_mov_b32_e32 v16, v5
	v_mov_b32_e32 v17, v9
	v_mov_b32_e32 v14, v4
	v_mov_b32_e32 v15, v8
	v_pk_mul_f32 v[16:17], v[16:17], v[16:17]
	v_mov_b32_e32 v18, v7
	v_mov_b32_e32 v19, v11
	v_pk_fma_f32 v[14:15], v[14:15], v[14:15], v[16:17]
	v_mov_b32_e32 v16, v6
	v_mov_b32_e32 v17, v10
	v_pk_mul_f32 v[18:19], v[18:19], v[18:19]
	s_nop 0
	v_pk_fma_f32 v[16:17], v[16:17], v[16:17], v[18:19]
	s_nop 0
	v_pk_add_f32 v[14:15], v[14:15], v[16:17]
	s_nop 0
	v_add_f32_e32 v2, v15, v12
	v_add_f32_e32 v12, v14, v2

.LBB0_268:
	s_or_b64 exec, exec, s[4:5]
	s_andn2_b64 vcc, exec, s[60:61]
	s_cbranch_vccnz .LBB0_270
	s_waitcnt lgkmcnt(0)
	v_lshlrev_b64 v[12:13], 7, v[20:21]
	v_lshl_add_u64 v[12:13], s[18:19], 0, v[12:13]
	v_lshlrev_b32_e32 v2, 2, v147
	v_lshl_add_u64 v[12:13], v[12:13], 0, v[2:3]
	global_store_dwordx4 v[12:13], v[8:11], off nt
	global_store_dwordx4 v[12:13], v[4:7], off offset:16 nt

.LBB0_292:
	s_lshl_b32 s4, s20, 8
	v_mov_b32_e32 v152, v0
	s_add_i32 s4, s4, s52
	v_cvt_pk_bf16_f32 v72, v72, v73
	v_and_or_b32 v142, v152, 15, s4
	s_lshl_b32 s4, s60, 8
	v_lshrrev_b32_e32 v152, 1, v152
	s_or_b32 s4, s4, s53
	v_ashrrev_i32_e32 v143, 31, v142
	v_and_or_b32 v152, v152, 24, s4
	v_or_b32_e32 v144, 16, v142
	v_or_b32_e32 v148, 32, v142
	v_or_b32_e32 v150, 48, v142
	v_ashrrev_i32_e32 v153, 31, v152
	v_lshlrev_b64 v[142:143], 11, v[142:143]
	v_lshl_add_u64 v[142:143], s[14:15], 0, v[142:143]
	v_lshlrev_b64 v[152:153], 1, v[152:153]
	v_lshl_add_u64 v[142:143], v[142:143], 0, v[152:153]
	s_mov_b64 s[4:5], 0x40000
	v_cvt_pk_bf16_f32 v73, v74, v75
	v_cvt_pk_bf16_f32 v74, v68, v69
	v_lshl_add_u64 v[68:69], v[142:143], 0, s[4:5]
	s_mov_b32 s4, 0x40000
	v_cvt_pk_bf16_f32 v64, v64, v65
	v_cvt_pk_bf16_f32 v65, v66, v67
	v_cvt_pk_bf16_f32 v66, v60, v61
	v_add_co_u32_e32 v60, vcc, s4, v142
	v_cvt_pk_bf16_f32 v48, v48, v49
	v_cvt_pk_bf16_f32 v49, v50, v51
	v_cvt_pk_bf16_f32 v50, v44, v45
	v_cvt_pk_bf16_f32 v51, v46, v47
	s_mov_b64 s[4:5], 0x48000
	v_addc_co_u32_e32 v61, vcc, 0, v143, vcc
	global_store_dwordx4 v[68:69], v[48:51], off offset:256 nt
	v_cvt_pk_bf16_f32 v32, v32, v33
	v_cvt_pk_bf16_f32 v33, v34, v35
	v_lshl_add_u64 v[48:49], v[142:143], 0, s[4:5]
	s_mov_b32 s4, 0x48000
	v_add_co_u32_e32 v50, vcc, s4, v142
	v_cvt_pk_bf16_f32 v34, v28, v29
	v_cvt_pk_bf16_f32 v35, v30, v31
	s_mov_b64 s[4:5], 0x50000
	v_ashrrev_i32_e32 v145, 31, v144
	v_addc_co_u32_e32 v51, vcc, 0, v143, vcc
	global_store_dwordx4 v[48:49], v[32:35], off offset:256 nt
	v_ashrrev_i32_e32 v149, 31, v148
	v_cvt_pk_bf16_f32 v112, v112, v113
	v_lshl_add_u64 v[32:33], v[142:143], 0, s[4:5]
	s_mov_b32 s4, 0x50000
	v_cvt_pk_bf16_f32 v113, v114, v115
	v_cvt_pk_bf16_f32 v114, v108, v109
	v_lshlrev_b64 v[108:109], 11, v[144:145]
	v_add_co_u32_e32 v34, vcc, s4, v142
	v_cvt_pk_bf16_f32 v16, v16, v17
	v_cvt_pk_bf16_f32 v17, v18, v19
	v_cvt_pk_bf16_f32 v18, v12, v13
	v_cvt_pk_bf16_f32 v19, v14, v15
	s_mov_b64 s[4:5], 0x58000
	v_ashrrev_i32_e32 v151, 31, v150
	v_cvt_pk_bf16_f32 v115, v110, v111
	v_lshl_add_u64 v[108:109], s[14:15], 0, v[108:109]
	v_cvt_pk_bf16_f32 v96, v96, v97
	v_cvt_pk_bf16_f32 v97, v98, v99
	v_cvt_pk_bf16_f32 v98, v92, v93
	v_lshlrev_b64 v[92:93], 11, v[148:149]
	v_addc_co_u32_e32 v35, vcc, 0, v143, vcc
	global_store_dwordx4 v[32:33], v[16:19], off offset:256 nt
	global_store_dwordx4 v[142:143], v[112:115], off offset:256 nt
	v_cvt_pk_bf16_f32 v99, v94, v95
	v_lshl_add_u64 v[16:17], v[142:143], 0, s[4:5]
	s_mov_b32 s4, 0x58000
	v_lshl_add_u64 v[112:113], v[108:109], 0, v[152:153]
	v_lshl_add_u64 v[92:93], s[14:15], 0, v[92:93]
	v_cvt_pk_bf16_f32 v80, v80, v81
	v_cvt_pk_bf16_f32 v81, v82, v83
	v_cvt_pk_bf16_f32 v82, v76, v77
	v_lshlrev_b64 v[76:77], 11, v[150:151]
	v_add_co_u32_e32 v18, vcc, s4, v142
	global_store_dwordx4 v[112:113], v[96:99], off offset:256 nt
	v_cvt_pk_bf16_f32 v83, v78, v79
	v_lshl_add_u64 v[76:77], s[14:15], 0, v[76:77]
	v_lshl_add_u64 v[96:97], v[92:93], 0, v[152:153]
	v_addc_co_u32_e32 v19, vcc, 0, v143, vcc
	v_cvt_pk_bf16_f32 v128, v128, v129
	v_cvt_pk_bf16_f32 v129, v130, v131
	v_cvt_pk_bf16_f32 v130, v124, v125
	v_cvt_pk_bf16_f32 v131, v126, v127
	v_cvt_pk_bf16_f32 v108, v120, v121
	v_cvt_pk_bf16_f32 v109, v122, v123
	v_cvt_pk_bf16_f32 v110, v116, v117
	v_cvt_pk_bf16_f32 v111, v118, v119
	v_cvt_pk_bf16_f32 v92, v104, v105
	v_cvt_pk_bf16_f32 v93, v106, v107
	v_cvt_pk_bf16_f32 v94, v100, v101
	v_cvt_pk_bf16_f32 v95, v102, v103
	global_store_dwordx4 v[96:97], v[80:83], off offset:256 nt
	v_cvt_pk_bf16_f32 v78, v84, v85
	v_cvt_pk_bf16_f32 v79, v86, v87
	v_lshl_add_u64 v[80:81], v[76:77], 0, v[152:153]
	v_cvt_pk_bf16_f32 v76, v88, v89
	v_cvt_pk_bf16_f32 v77, v90, v91
	v_cvt_pk_bf16_f32 v75, v70, v71
	v_cvt_pk_bf16_f32 v67, v62, v63
	v_cvt_pk_bf16_f32 v44, v56, v57
	v_cvt_pk_bf16_f32 v45, v58, v59
	v_cvt_pk_bf16_f32 v46, v52, v53
	v_cvt_pk_bf16_f32 v47, v54, v55
	v_cvt_pk_bf16_f32 v28, v40, v41
	v_cvt_pk_bf16_f32 v29, v42, v43
	v_cvt_pk_bf16_f32 v30, v36, v37
	v_cvt_pk_bf16_f32 v31, v38, v39
	v_cvt_pk_bf16_f32 v12, v24, v25
	v_cvt_pk_bf16_f32 v13, v26, v27
	v_cvt_pk_bf16_f32 v14, v20, v21
	v_cvt_pk_bf16_f32 v15, v22, v23
	v_cvt_pk_bf16_f32 v8, v8, v9
	v_cvt_pk_bf16_f32 v9, v10, v11
	v_cvt_pk_bf16_f32 v10, v4, v5
	v_cvt_pk_bf16_f32 v11, v6, v7
	s_andn2_b64 vcc, exec, s[22:23]
	s_mov_b64 s[4:5], -1
	global_store_dwordx4 v[142:143], v[128:131], off nt
	global_store_dwordx4 v[112:113], v[108:111], off nt
	global_store_dwordx4 v[96:97], v[92:95], off nt
	global_store_dwordx4 v[80:81], v[76:79], off nt
	global_store_dwordx4 v[80:81], v[72:75], off offset:256 nt
	global_store_dwordx4 v[60:61], v[64:67], off nt
	global_store_dwordx4 v[50:51], v[44:47], off nt
	global_store_dwordx4 v[34:35], v[28:31], off nt
	global_store_dwordx4 v[18:19], v[12:15], off nt
	global_store_dwordx4 v[16:17], v[8:11], off offset:256 nt
	s_cbranch_vccnz .LBB0_281
	s_andn2_b64 vcc, exec, s[10:11]
	s_cbranch_vccnz .LBB0_280
	s_barrier
	s_branch .LBB0_280
